# O2 spatial-gating epilogue: 4x4 transpose across lane rows (permlane16/32 swap) and 4 dwordx4 stores instead of 16 dword stores per trip; counted vmcnt waits adjusted
# speedup vs baseline: 1.0143x; 1.0094x over previous
; #define LAS __attribute__((address_space(3)))
; __device__ __forceinline__ void phase_sgu(CArgs a, LAS unsigned char* lds, int i2, int wv, int xw  ) {
;     ...
;             u32x2 uvp[4][4]; float bsp[4];
; #pragma unroll
;             for (int m = 0; m < 4; ++m) bsp[m] = a->in[I_SGUB][((size_t)i2 * 8 + h) * 128 + wr * 64 + m * 16 + fr];
; #pragma unroll
;             for (int m = 0; m < 4; ++m)
; #pragma unroll
;                 for (int n = 0; n < 4; ++n) uvp[m][n] = *(const u32x2*)(HB + (tok0 + wr * 64 + m * 16 + fr) * (2 * SGU_W) + h * 256 + wc * 64 + n * 16 + 4 * fq);
;             f32x4 acc[4][4];
; #pragma unroll
;             for (int m = 0; m < 4; ++m)
; #pragma unroll
;                 for (int n = 0; n < 4; ++n) acc[m][n] = (f32x4){0.f, 0.f, 0.f, 0.f};
; #pragma unroll
;             for (int ks = 0; ks < 4; ++ks) {
;                 bf16x8 bfr[4], af[4];
; #pragma unroll
;                 for (int m = 0; m < 4; ++m) { const int i = wr * 64 + m * 16 + fr; af[m] = *(const LAS bf16x8*)(wl + i * 256 + (((ks * 4 + fq) ^ (i & 15)) * 16)); }
; #pragma unroll
;                 for (int n = 0; n < 4; ++n) bfr[n] = *(const LAS bf16x8*)(vt + (wc * 64 + n * 16 + fr) * VS + ks * 32 + fq * 8);
; #pragma unroll
;                 for (int m = 0; m < 4; ++m)
; #pragma unroll
;                     for (int n = 0; n < 4; ++n) acc[m][n] = __builtin_amdgcn_mfma_f32_16x16x32_bf16(bfr[n], af[m], acc[m][n], 0, 0, 0);
;             }
.LBB0_283:
	s_waitcnt vmcnt(0)
	s_waitcnt lgkmcnt(0)
	s_barrier
	s_load_dwordx2 s[22:23], s[2:3], 0x88
	s_add_u32 s6, s6, 0x400
	s_addc_u32 s7, s7, 0
	v_lshl_add_u64 v[116:117], v[116:117], 0, s[60:61]
	v_lshl_add_u64 v[122:123], v[122:123], 0, s[60:61]
	s_waitcnt lgkmcnt(0)
	v_lshl_add_u64 v[32:33], s[22:23], 0, v[132:133]
	global_load_dword v168, v[32:33], off
	global_load_dword v156, v[32:33], off offset:64
	global_load_dword v144, v[32:33], off offset:128
	global_load_dword v134, v[32:33], off offset:192
	v_lshl_add_u64 v[32:33], s[4:5], 0, v[120:121]
	v_add_co_u32_e32 v34, vcc, s71, v32
	s_mov_b32 s22, 0x3a020000
	s_nop 0
	v_addc_co_u32_e32 v35, vcc, 0, v33, vcc
	global_load_dwordx2 v[174:175], v[34:35], off
	global_load_dwordx2 v[172:173], v[34:35], off offset:32
	global_load_dwordx2 v[170:171], v[34:35], off offset:64
	global_load_dwordx2 v[166:167], v[34:35], off offset:96
	v_add_co_u32_e32 v34, vcc, s22, v32
	s_mov_b32 s22, 0x3a040000
	s_nop 0
	v_addc_co_u32_e32 v35, vcc, 0, v33, vcc
	global_load_dwordx2 v[164:165], v[34:35], off
	global_load_dwordx2 v[162:163], v[34:35], off offset:32
	global_load_dwordx2 v[160:161], v[34:35], off offset:64
	global_load_dwordx2 v[158:159], v[34:35], off offset:96
	v_add_co_u32_e32 v34, vcc, s22, v32
	s_mov_b32 s22, 0x3a060000
	s_nop 0
	v_addc_co_u32_e32 v35, vcc, 0, v33, vcc
	v_add_co_u32_e32 v32, vcc, s22, v32
	global_load_dwordx2 v[154:155], v[34:35], off
	global_load_dwordx2 v[150:151], v[34:35], off offset:32
	global_load_dwordx2 v[148:149], v[34:35], off offset:64
	global_load_dwordx2 v[146:147], v[34:35], off offset:96
	v_addc_co_u32_e32 v33, vcc, 0, v33, vcc
	global_load_dwordx2 v[142:143], v[32:33], off
	global_load_dwordx2 v[140:141], v[32:33], off offset:32
	global_load_dwordx2 v[138:139], v[32:33], off offset:64
	global_load_dwordx2 v[136:137], v[32:33], off offset:96
	ds_read_b128 v[32:35], v196
	ds_read_b128 v[40:43], v196 offset:4096
	ds_read_b128 v[56:59], v196 offset:8192
	ds_read_b128 v[72:75], v196 offset:12288
	ds_read_b128 v[60:63], v197
	ds_read_b128 v[64:67], v197 offset:4352
	ds_read_b128 v[68:71], v197 offset:8704
	ds_read_b128 v[80:83], v197 offset:13056
	s_waitcnt lgkmcnt(3)
	v_mfma_f32_16x16x32_bf16 v[108:111], v[60:63], v[32:35], 0
	s_movk_i32 s22, 0xc0
	v_lshl_add_u64 v[120:121], v[120:121], 0, s[62:63]
	v_lshl_add_u64 v[124:125], v[124:125], 0, s[60:61]
	s_waitcnt lgkmcnt(2)
	v_mfma_f32_16x16x32_bf16 v[104:107], v[64:67], v[32:35], 0
	v_lshl_add_u64 v[126:127], v[126:127], 0, s[60:61]
	v_lshl_add_u64 v[128:129], v[128:129], 0, s[62:63]
	v_lshl_add_u64 v[130:131], v[130:131], 0, s[62:63]
	s_waitcnt lgkmcnt(1)
	v_mfma_f32_16x16x32_bf16 v[96:99], v[68:71], v[32:35], 0
	v_lshl_add_u64 v[132:133], v[132:133], 0, s[62:63]
	s_waitcnt lgkmcnt(0)
	v_mfma_f32_16x16x32_bf16 v[88:91], v[80:83], v[32:35], 0
	v_mfma_f32_16x16x32_bf16 v[76:79], v[60:63], v[40:43], 0
	v_mfma_f32_16x16x32_bf16 v[32:35], v[64:67], v[40:43], 0
	v_mfma_f32_16x16x32_bf16 v[36:39], v[68:71], v[40:43], 0
	v_mfma_f32_16x16x32_bf16 v[40:43], v[80:83], v[40:43], 0
	v_mfma_f32_16x16x32_bf16 v[44:47], v[60:63], v[56:59], 0
	v_mfma_f32_16x16x32_bf16 v[48:51], v[64:67], v[56:59], 0
	v_mfma_f32_16x16x32_bf16 v[52:55], v[68:71], v[56:59], 0
	v_mfma_f32_16x16x32_bf16 v[56:59], v[80:83], v[56:59], 0
	v_mfma_f32_16x16x32_bf16 v[60:63], v[60:63], v[72:75], 0
	v_mfma_f32_16x16x32_bf16 v[64:67], v[64:67], v[72:75], 0
	v_mfma_f32_16x16x32_bf16 v[68:71], v[68:71], v[72:75], 0
	v_mfma_f32_16x16x32_bf16 v[72:75], v[80:83], v[72:75], 0
	ds_read_b128 v[100:103], v198
	ds_read_b128 v[92:95], v198 offset:4096
	ds_read_b128 v[84:87], v198 offset:8192
	ds_read_b128 v[80:83], v198 offset:12288
	ds_read_b128 v[202:205], v197 offset:64
	ds_read_b128 v[206:209], v197 offset:4416
	ds_read_b128 v[210:213], v197 offset:8768
	ds_read_b128 v[214:217], v197 offset:13120
	s_waitcnt lgkmcnt(3)
	v_mfma_f32_16x16x32_bf16 v[108:111], v[202:205], v[100:103], v[108:111]
	s_waitcnt lgkmcnt(2)
	v_mfma_f32_16x16x32_bf16 v[104:107], v[206:209], v[100:103], v[104:107]
	s_waitcnt lgkmcnt(1)
	v_mfma_f32_16x16x32_bf16 v[96:99], v[210:213], v[100:103], v[96:99]
	s_waitcnt lgkmcnt(0)
	v_mfma_f32_16x16x32_bf16 v[88:91], v[214:217], v[100:103], v[88:91]
	v_mfma_f32_16x16x32_bf16 v[76:79], v[202:205], v[92:95], v[76:79]
	v_mfma_f32_16x16x32_bf16 v[32:35], v[206:209], v[92:95], v[32:35]
	v_mfma_f32_16x16x32_bf16 v[36:39], v[210:213], v[92:95], v[36:39]
	v_mfma_f32_16x16x32_bf16 v[40:43], v[214:217], v[92:95], v[40:43]
	v_mfma_f32_16x16x32_bf16 v[44:47], v[202:205], v[84:87], v[44:47]
	v_mfma_f32_16x16x32_bf16 v[48:51], v[206:209], v[84:87], v[48:51]
	v_mfma_f32_16x16x32_bf16 v[52:55], v[210:213], v[84:87], v[52:55]
	v_mfma_f32_16x16x32_bf16 v[56:59], v[214:217], v[84:87], v[56:59]
	v_mfma_f32_16x16x32_bf16 v[60:63], v[202:205], v[80:83], v[60:63]
	v_mfma_f32_16x16x32_bf16 v[64:67], v[206:209], v[80:83], v[64:67]
	v_mfma_f32_16x16x32_bf16 v[68:71], v[210:213], v[80:83], v[68:71]
	v_mfma_f32_16x16x32_bf16 v[72:75], v[214:217], v[80:83], v[72:75]
	ds_read_b128 v[80:83], v199
	ds_read_b128 v[84:87], v199 offset:4096
	ds_read_b128 v[92:95], v199 offset:8192
	ds_read_b128 v[100:103], v199 offset:12288
	ds_read_b128 v[202:205], v197 offset:128
	ds_read_b128 v[206:209], v197 offset:4480
	ds_read_b128 v[210:213], v197 offset:8832
	ds_read_b128 v[214:217], v197 offset:13184
	s_waitcnt lgkmcnt(3)
	v_mfma_f32_16x16x32_bf16 v[108:111], v[202:205], v[80:83], v[108:111]
	s_waitcnt lgkmcnt(2)
	v_mfma_f32_16x16x32_bf16 v[104:107], v[206:209], v[80:83], v[104:107]
	s_waitcnt lgkmcnt(1)
	v_mfma_f32_16x16x32_bf16 v[96:99], v[210:213], v[80:83], v[96:99]
	s_waitcnt lgkmcnt(0)
; __device__ __forceinline__ void phase_sgu(CArgs a, LAS unsigned char* lds, int i2, int wv, int xw  ) {
;     ...
;                 for (int m = 0; m < 4; ++m)
; #pragma unroll
;                     for (int n = 0; n < 4; ++n) acc[m][n] = __builtin_amdgcn_mfma_f32_16x16x32_bf16(bfr[n], af[m], acc[m][n], 0, 0, 0);
;             }
;             { int te = tz; asm volatile("" : "+v"(te));
;               const int le = te & 63, we = te >> 6, wr = we >> 2, wc = we & 3, fr = le & 15, fq = le >> 4;
; #pragma unroll
;             for (int m = 0; m < 4; ++m) { const int i = wr * 64 + m * 16 + fr; const float bs = bsp[m];
; #pragma unroll
;                 for (int n = 0; n < 4; ++n) { const int cc = h * 256 + wc * 64 + n * 16 + 4 * fq;
;                     const f32x4 sv = acc[m][n] + bs; const u32x2 uv = uvp[m][n];
;                     *(unsigned*)(YQ + (tok0 + i) * SGU_W + cc) = pk4_fp8(bflo(uv.x) * sv.x * QS_GATED, bfhi(uv.x) * sv.y * QS_GATED, bflo(uv.y) * sv.z * QS_GATED, bfhi(uv.y) * sv.w * QS_GATED); } } }
	v_mfma_f32_16x16x32_bf16 v[80:83], v[214:217], v[80:83], v[88:91]
	v_mfma_f32_16x16x32_bf16 v[76:79], v[202:205], v[84:87], v[76:79]
	v_mfma_f32_16x16x32_bf16 v[32:35], v[206:209], v[84:87], v[32:35]
	v_mfma_f32_16x16x32_bf16 v[36:39], v[210:213], v[84:87], v[36:39]
	v_mfma_f32_16x16x32_bf16 v[40:43], v[214:217], v[84:87], v[40:43]
	v_mfma_f32_16x16x32_bf16 v[44:47], v[202:205], v[92:95], v[44:47]
	v_mfma_f32_16x16x32_bf16 v[48:51], v[206:209], v[92:95], v[48:51]
	v_mfma_f32_16x16x32_bf16 v[52:55], v[210:213], v[92:95], v[52:55]
	v_mfma_f32_16x16x32_bf16 v[84:87], v[214:217], v[92:95], v[56:59]
	v_mfma_f32_16x16x32_bf16 v[88:91], v[202:205], v[100:103], v[60:63]
	v_mfma_f32_16x16x32_bf16 v[92:95], v[206:209], v[100:103], v[64:67]
	v_mfma_f32_16x16x32_bf16 v[202:205], v[210:213], v[100:103], v[68:71]
	v_mfma_f32_16x16x32_bf16 v[100:103], v[214:217], v[100:103], v[72:75]
	ds_read_b128 v[56:59], v200
	ds_read_b128 v[60:63], v200 offset:4096
	ds_read_b128 v[206:209], v200 offset:8192
	ds_read_b128 v[210:213], v200 offset:12288
	ds_read_b128 v[214:217], v197 offset:192
	ds_read_b128 v[218:221], v197 offset:4544
	ds_read_b128 v[222:225], v197 offset:8896
	ds_read_b128 v[226:229], v197 offset:13248
	s_waitcnt lgkmcnt(3)
	v_mfma_f32_16x16x32_bf16 v[108:111], v[214:217], v[56:59], v[108:111]
	s_waitcnt lgkmcnt(2)
	v_mfma_f32_16x16x32_bf16 v[104:107], v[218:221], v[56:59], v[104:107]
	s_waitcnt lgkmcnt(1)
	v_mfma_f32_16x16x32_bf16 v[96:99], v[222:225], v[56:59], v[96:99]
	s_waitcnt lgkmcnt(0)
	v_mfma_f32_16x16x32_bf16 v[80:83], v[226:229], v[56:59], v[80:83]
	v_mfma_f32_16x16x32_bf16 v[56:59], v[218:221], v[206:209], v[48:51]
	v_mfma_f32_16x16x32_bf16 v[48:51], v[226:229], v[206:209], v[84:87]
	s_waitcnt vmcnt(19)
	s_nop 4
	v_pk_add_f32 v[80:81], v[168:169], v[80:81] op_sel_hi:[0,1]
	v_pk_add_f32 v[82:83], v[168:169], v[82:83] op_sel_hi:[0,1]
	s_waitcnt vmcnt(17)
	v_pk_add_f32 v[56:57], v[144:145], v[56:57] op_sel_hi:[0,1]
	v_mov_b32_e32 v85, v112
	v_bfe_u32 v248, v112, 4, 2
	v_mov_b32_e32 v249, 0
	v_mul_u32_u24_e32 v248, 12, v248
	v_mfma_f32_16x16x32_bf16 v[76:79], v[214:217], v[60:63], v[76:79]
	v_and_b32_e32 v84, 15, v85
	v_ashrrev_i32_e32 v86, 2, v85
	v_and_or_b32 v84, v86, s39, v84
	v_lshrrev_b32_e32 v86, 2, v85
	v_and_b32_e32 v86, 12, v86
	v_and_or_b32 v85, v85, s22, v86
	v_add_u32_e32 v152, s24, v85
	v_ashrrev_i32_e32 v85, 31, v84
	v_mfma_f32_16x16x32_bf16 v[72:75], v[218:221], v[60:63], v[32:35]
	v_lshl_add_u64 v[86:87], s[20:21], 0, v[84:85]
	s_waitcnt vmcnt(15)
	v_lshlrev_b32_e32 v85, 16, v174
	v_lshlrev_b64 v[86:87], 11, v[86:87]
	v_mfma_f32_16x16x32_bf16 v[68:71], v[222:225], v[60:63], v[36:39]
	v_lshl_add_u64 v[86:87], s[10:11], 0, v[86:87]
	v_lshl_add_u64 v[86:87], v[86:87], 0, v[152:153]
	v_pk_add_f32 v[76:77], v[156:157], v[76:77] op_sel_hi:[0,1]
	v_mfma_f32_16x16x32_bf16 v[64:67], v[226:229], v[60:63], v[40:43]
	v_add_f32_e64 v78, v156, v78
	v_add_f32_e64 v79, v156, v79
	v_pk_add_f32 v[72:73], v[156:157], v[72:73] op_sel_hi:[0,1]
	v_pk_add_f32 v[74:75], v[156:157], v[74:75] op_sel_hi:[0,1]
	v_mfma_f32_16x16x32_bf16 v[60:63], v[214:217], v[206:209], v[44:47]
	v_add_f32_e64 v68, v156, v68
	v_add_f32_e64 v69, v156, v69
	v_pk_add_f32 v[70:71], v[156:157], v[70:71] op_sel_hi:[0,1]
	v_pk_add_f32 v[64:65], v[156:157], v[64:65] op_sel_hi:[0,1]
	v_mfma_f32_16x16x32_bf16 v[44:47], v[214:217], v[210:213], v[88:91]
	v_add_f32_e64 v66, v156, v66
	v_add_f32_e64 v67, v156, v67
	s_nop 0
	v_pk_add_f32 v[60:61], v[144:145], v[60:61] op_sel_hi:[0,1]
	v_pk_add_f32 v[62:63], v[144:145], v[62:63] op_sel_hi:[0,1]
	v_pk_add_f32 v[90:91], v[168:169], v[108:109] op_sel_hi:[0,1]
	v_mul_f32_e32 v85, v90, v85
	v_and_b32_e32 v90, 0xffff0000, v174
	v_pk_add_f32 v[88:89], v[168:169], v[110:111] op_sel_hi:[0,1]
	v_mul_f32_e32 v90, v91, v90
	v_lshlrev_b32_e32 v91, 16, v175
	v_mul_f32_e32 v85, 0x41000000, v85
	v_mul_f32_e32 v90, 0x41000000, v90
	v_mul_f32_e32 v88, v88, v91
	v_and_b32_e32 v91, 0xffff0000, v175
	v_mul_f32_e32 v89, v89, v91
	v_med3_f32 v85, v85, s51, v187
	v_med3_f32 v90, v90, s51, v187
	v_cvt_pk_fp8_f32 v232, v85, v90
	v_mul_f32_e32 v88, 0x41000000, v88
	v_mul_f32_e32 v89, 0x41000000, v89
	v_med3_f32 v88, v88, s51, v187
	v_med3_f32 v89, v89, s51, v187
	v_cvt_pk_fp8_f32 v232, v88, v89 op_sel:[0,0,1]
	s_waitcnt vmcnt(14)
	v_lshlrev_b32_e32 v85, 16, v172
	v_pk_add_f32 v[88:89], v[168:169], v[106:107] op_sel_hi:[0,1]
	v_mfma_f32_16x16x32_bf16 v[52:55], v[222:225], v[206:209], v[52:55]
	v_pk_add_f32 v[90:91], v[168:169], v[104:105] op_sel_hi:[0,1]
	v_mul_f32_e32 v85, v90, v85
	v_and_b32_e32 v90, 0xffff0000, v172
	v_mul_f32_e32 v90, v91, v90
	v_lshlrev_b32_e32 v91, 16, v173
	v_mul_f32_e32 v85, 0x41000000, v85
	v_mul_f32_e32 v90, 0x41000000, v90
	v_mul_f32_e32 v88, v88, v91
	v_and_b32_e32 v91, 0xffff0000, v173
	v_mul_f32_e32 v89, v89, v91
	v_med3_f32 v85, v85, s51, v187
	v_med3_f32 v90, v90, s51, v187
	v_cvt_pk_fp8_f32 v233, v85, v90
	v_mul_f32_e32 v88, 0x41000000, v88
	v_mul_f32_e32 v89, 0x41000000, v89
	v_med3_f32 v88, v88, s51, v187
	v_med3_f32 v89, v89, s51, v187
	v_cvt_pk_fp8_f32 v233, v88, v89 op_sel:[0,0,1]
	s_waitcnt vmcnt(13)
	v_lshlrev_b32_e32 v85, 16, v170
	v_pk_add_f32 v[88:89], v[168:169], v[98:99] op_sel_hi:[0,1]
	v_pk_add_f32 v[58:59], v[144:145], v[58:59] op_sel_hi:[0,1]
	v_pk_add_f32 v[90:91], v[168:169], v[96:97] op_sel_hi:[0,1]
	v_mul_f32_e32 v85, v90, v85
	v_and_b32_e32 v90, 0xffff0000, v170
	v_mul_f32_e32 v90, v91, v90
	v_lshlrev_b32_e32 v91, 16, v171
	v_mul_f32_e32 v85, 0x41000000, v85
	v_mul_f32_e32 v90, 0x41000000, v90
	v_mul_f32_e32 v88, v88, v91
	v_and_b32_e32 v91, 0xffff0000, v171
	v_mul_f32_e32 v89, v89, v91
	v_med3_f32 v85, v85, s51, v187
	v_med3_f32 v90, v90, s51, v187
	v_cvt_pk_fp8_f32 v234, v85, v90
	s_waitcnt vmcnt(12)
; __device__ __forceinline__ void phase_sgu(CArgs a, LAS unsigned char* lds, int i2, int wv, int xw  ) {
;     ...
;             for (int m = 0; m < 4; ++m) { const int i = wr * 64 + m * 16 + fr; const float bs = bsp[m];
; #pragma unroll
;                 for (int n = 0; n < 4; ++n) { const int cc = h * 256 + wc * 64 + n * 16 + 4 * fq;
;                     const f32x4 sv = acc[m][n] + bs; const u32x2 uv = uvp[m][n];
;                     *(unsigned*)(YQ + (tok0 + i) * SGU_W + cc) = pk4_fp8(bflo(uv.x) * sv.x * QS_GATED, bfhi(uv.x) * sv.y * QS_GATED, bflo(uv.y) * sv.z * QS_GATED, bfhi(uv.y) * sv.w * QS_GATED); } } }
	v_lshlrev_b32_e32 v85, 16, v166
	v_mul_f32_e32 v80, v80, v85
	v_and_b32_e32 v85, 0xffff0000, v166
	v_mul_f32_e32 v81, v81, v85
	v_lshlrev_b32_e32 v85, 16, v167
	v_mul_f32_e32 v80, 0x41000000, v80
	v_mul_f32_e32 v81, 0x41000000, v81
	v_mul_f32_e32 v82, v82, v85
	v_and_b32_e32 v85, 0xffff0000, v167
	v_mul_f32_e32 v83, v83, v85
	v_med3_f32 v80, v80, s51, v187
	v_med3_f32 v81, v81, s51, v187
	v_cvt_pk_fp8_f32 v235, v80, v81
	v_mul_f32_e32 v82, 0x41000000, v82
	v_mul_f32_e32 v83, 0x41000000, v83
	v_med3_f32 v82, v82, s51, v187
	v_med3_f32 v83, v83, s51, v187
	v_cvt_pk_fp8_f32 v235, v82, v83 op_sel:[0,0,1]
	s_waitcnt vmcnt(11)
	v_lshlrev_b32_e32 v82, 16, v164
	v_mul_f32_e32 v76, v76, v82
	v_and_b32_e32 v82, 0xffff0000, v164
	v_mul_f32_e32 v77, v77, v82
	v_lshlrev_b32_e32 v82, 16, v165
	v_mul_f32_e32 v76, 0x41000000, v76
	v_mul_f32_e32 v77, 0x41000000, v77
	v_mul_f32_e32 v78, v78, v82
	v_and_b32_e32 v82, 0xffff0000, v165
	v_mul_f32_e32 v79, v79, v82
	v_med3_f32 v76, v76, s51, v187
	v_med3_f32 v77, v77, s51, v187
	v_cvt_pk_fp8_f32 v236, v76, v77
	v_mul_f32_e32 v78, 0x41000000, v78
	v_mul_f32_e32 v79, 0x41000000, v79
	v_med3_f32 v78, v78, s51, v187
	v_med3_f32 v79, v79, s51, v187
	v_cvt_pk_fp8_f32 v236, v78, v79 op_sel:[0,0,1]
	s_waitcnt vmcnt(10)
	v_lshlrev_b32_e32 v78, 16, v162
	v_mul_f32_e32 v72, v72, v78
	v_and_b32_e32 v78, 0xffff0000, v162
	v_mul_f32_e32 v73, v73, v78
	v_lshlrev_b32_e32 v78, 16, v163
	v_mul_f32_e32 v72, 0x41000000, v72
	v_mul_f32_e32 v73, 0x41000000, v73
	v_mul_f32_e32 v74, v74, v78
	v_and_b32_e32 v78, 0xffff0000, v163
	v_mul_f32_e32 v75, v75, v78
	v_med3_f32 v72, v72, s51, v187
	v_med3_f32 v73, v73, s51, v187
	v_cvt_pk_fp8_f32 v237, v72, v73
	s_waitcnt vmcnt(9)
	v_lshlrev_b32_e32 v72, 16, v160
	v_mul_f32_e32 v68, v68, v72
	v_and_b32_e32 v72, 0xffff0000, v160
	v_mul_f32_e32 v69, v69, v72
	v_lshlrev_b32_e32 v72, 16, v161
	v_mul_f32_e32 v68, 0x41000000, v68
	v_mul_f32_e32 v69, 0x41000000, v69
	v_mul_f32_e32 v70, v70, v72
	v_and_b32_e32 v72, 0xffff0000, v161
	v_mul_f32_e32 v71, v71, v72
	v_med3_f32 v68, v68, s51, v187
	v_med3_f32 v69, v69, s51, v187
	v_cvt_pk_fp8_f32 v238, v68, v69
	s_waitcnt vmcnt(8)
	v_lshlrev_b32_e32 v68, 16, v158
	v_mul_f32_e32 v64, v64, v68
	v_and_b32_e32 v68, 0xffff0000, v158
	v_mul_f32_e32 v65, v65, v68
	v_lshlrev_b32_e32 v68, 16, v159
	v_mul_f32_e32 v64, 0x41000000, v64
	v_mul_f32_e32 v65, 0x41000000, v65
	v_mul_f32_e32 v66, v66, v68
	v_and_b32_e32 v68, 0xffff0000, v159
	v_mul_f32_e32 v67, v67, v68
	v_med3_f32 v64, v64, s51, v187
	v_med3_f32 v65, v65, s51, v187
	v_cvt_pk_fp8_f32 v239, v64, v65
	v_mul_f32_e32 v66, 0x41000000, v66
	v_mul_f32_e32 v67, 0x41000000, v67
	v_med3_f32 v66, v66, s51, v187
	v_med3_f32 v67, v67, s51, v187
	v_cvt_pk_fp8_f32 v239, v66, v67 op_sel:[0,0,1]
	s_waitcnt vmcnt(7)
	v_lshlrev_b32_e32 v66, 16, v154
	v_mul_f32_e32 v60, v60, v66
	v_and_b32_e32 v66, 0xffff0000, v154
	v_mul_f32_e32 v61, v61, v66
	v_lshlrev_b32_e32 v66, 16, v155
	v_mul_f32_e32 v60, 0x41000000, v60
	v_mul_f32_e32 v61, 0x41000000, v61
	v_mul_f32_e32 v62, v62, v66
	v_and_b32_e32 v66, 0xffff0000, v155
	v_mul_f32_e32 v63, v63, v66
	v_med3_f32 v60, v60, s51, v187
	v_med3_f32 v61, v61, s51, v187
	v_cvt_pk_fp8_f32 v240, v60, v61
	v_mul_f32_e32 v62, 0x41000000, v62
	v_mul_f32_e32 v63, 0x41000000, v63
	v_med3_f32 v62, v62, s51, v187
	v_med3_f32 v63, v63, s51, v187
	v_cvt_pk_fp8_f32 v240, v62, v63 op_sel:[0,0,1]
	s_waitcnt vmcnt(6)
	v_lshlrev_b32_e32 v62, 16, v150
	v_mul_f32_e32 v56, v56, v62
	v_and_b32_e32 v62, 0xffff0000, v150
	v_mul_f32_e32 v57, v57, v62
	v_lshlrev_b32_e32 v62, 16, v151
	v_mul_f32_e32 v56, 0x41000000, v56
	v_mul_f32_e32 v57, 0x41000000, v57
	v_mul_f32_e32 v58, v58, v62
	v_and_b32_e32 v62, 0xffff0000, v151
	v_mul_f32_e32 v59, v59, v62
	v_med3_f32 v56, v56, s51, v187
	v_med3_f32 v57, v57, s51, v187
	v_cvt_pk_fp8_f32 v241, v56, v57
	v_pk_add_f32 v[52:53], v[144:145], v[52:53] op_sel_hi:[0,1]
	s_waitcnt vmcnt(5)
	v_lshlrev_b32_e32 v56, 16, v148
	v_mul_f32_e32 v52, v52, v56
	v_and_b32_e32 v56, 0xffff0000, v148
	v_pk_add_f32 v[54:55], v[144:145], v[54:55] op_sel_hi:[0,1]
	v_mul_f32_e32 v53, v53, v56
	v_lshlrev_b32_e32 v56, 16, v149
	v_mul_f32_e32 v52, 0x41000000, v52
	v_mul_f32_e32 v53, 0x41000000, v53
	v_mul_f32_e32 v54, v54, v56
	v_and_b32_e32 v56, 0xffff0000, v149
	v_mul_f32_e32 v55, v55, v56
	v_med3_f32 v52, v52, s51, v187
	v_med3_f32 v53, v53, s51, v187
	v_cvt_pk_fp8_f32 v242, v52, v53
	v_pk_add_f32 v[48:49], v[144:145], v[48:49] op_sel_hi:[0,1]
	s_waitcnt vmcnt(4)
	v_lshlrev_b32_e32 v52, 16, v146
	v_mul_f32_e32 v48, v48, v52
	v_and_b32_e32 v52, 0xffff0000, v146
	v_pk_add_f32 v[50:51], v[144:145], v[50:51] op_sel_hi:[0,1]
	v_mul_f32_e32 v49, v49, v52
	v_lshlrev_b32_e32 v52, 16, v147
	v_mul_f32_e32 v48, 0x41000000, v48
	v_mul_f32_e32 v49, 0x41000000, v49
	v_mul_f32_e32 v50, v50, v52
	v_and_b32_e32 v52, 0xffff0000, v147
	v_mul_f32_e32 v51, v51, v52
	v_med3_f32 v48, v48, s51, v187
	v_med3_f32 v49, v49, s51, v187
	v_cvt_pk_fp8_f32 v243, v48, v49
	v_mul_f32_e32 v50, 0x41000000, v50
	v_mul_f32_e32 v51, 0x41000000, v51
	v_med3_f32 v50, v50, s51, v187
	v_med3_f32 v51, v51, s51, v187
	v_cvt_pk_fp8_f32 v243, v50, v51 op_sel:[0,0,1]
	v_pk_add_f32 v[44:45], v[134:135], v[44:45] op_sel_hi:[0,1]
	s_waitcnt vmcnt(3)
; __device__ __forceinline__ void phase_sgu(CArgs a, LAS unsigned char* lds, int i2, int wv, int xw  ) {
;     ...
;                 for (int m = 0; m < 4; ++m)
; #pragma unroll
;                     for (int n = 0; n < 4; ++n) acc[m][n] = __builtin_amdgcn_mfma_f32_16x16x32_bf16(bfr[n], af[m], acc[m][n], 0, 0, 0);
;             }
;             { int te = tz; asm volatile("" : "+v"(te));
;               const int le = te & 63, we = te >> 6, wr = we >> 2, wc = we & 3, fr = le & 15, fq = le >> 4;
; #pragma unroll
;             for (int m = 0; m < 4; ++m) { const int i = wr * 64 + m * 16 + fr; const float bs = bsp[m];
; #pragma unroll
;                 for (int n = 0; n < 4; ++n) { const int cc = h * 256 + wc * 64 + n * 16 + 4 * fq;
;                     const f32x4 sv = acc[m][n] + bs; const u32x2 uv = uvp[m][n];
;                     *(unsigned*)(YQ + (tok0 + i) * SGU_W + cc) = pk4_fp8(bflo(uv.x) * sv.x * QS_GATED, bfhi(uv.x) * sv.y * QS_GATED, bflo(uv.y) * sv.z * QS_GATED, bfhi(uv.y) * sv.w * QS_GATED); } } }
	v_lshlrev_b32_e32 v50, 16, v142
	v_mul_f32_e32 v44, v44, v50
	v_and_b32_e32 v50, 0xffff0000, v142
	v_pk_add_f32 v[46:47], v[134:135], v[46:47] op_sel_hi:[0,1]
	v_mul_f32_e32 v45, v45, v50
	v_lshlrev_b32_e32 v50, 16, v143
	v_mul_f32_e32 v44, 0x41000000, v44
	v_mul_f32_e32 v45, 0x41000000, v45
	v_mul_f32_e32 v46, v46, v50
	v_and_b32_e32 v50, 0xffff0000, v143
	v_mul_f32_e32 v47, v47, v50
	v_med3_f32 v44, v44, s51, v187
	v_med3_f32 v45, v45, s51, v187
	v_mfma_f32_16x16x32_bf16 v[40:43], v[218:221], v[210:213], v[92:95]
	v_cvt_pk_fp8_f32 v244, v44, v45
	v_mul_f32_e32 v46, 0x41000000, v46
	v_mul_f32_e32 v47, 0x41000000, v47
	v_med3_f32 v46, v46, s51, v187
	v_med3_f32 v47, v47, s51, v187
	v_cvt_pk_fp8_f32 v244, v46, v47 op_sel:[0,0,1]
	s_nop 1
	v_pk_add_f32 v[40:41], v[134:135], v[40:41] op_sel_hi:[0,1]
	s_waitcnt vmcnt(2)
	v_lshlrev_b32_e32 v46, 16, v140
	v_mfma_f32_16x16x32_bf16 v[36:39], v[222:225], v[210:213], v[202:205]
	v_mul_f32_e32 v40, v40, v46
	v_and_b32_e32 v46, 0xffff0000, v140
	v_pk_add_f32 v[42:43], v[134:135], v[42:43] op_sel_hi:[0,1]
	v_mul_f32_e32 v41, v41, v46
	v_lshlrev_b32_e32 v46, 16, v141
	v_mul_f32_e32 v40, 0x41000000, v40
	v_mul_f32_e32 v41, 0x41000000, v41
	v_mul_f32_e32 v42, v42, v46
	v_and_b32_e32 v46, 0xffff0000, v141
	v_mul_f32_e32 v43, v43, v46
	v_med3_f32 v40, v40, s51, v187
	v_med3_f32 v41, v41, s51, v187
	v_cvt_pk_fp8_f32 v245, v40, v41
	v_pk_add_f32 v[36:37], v[134:135], v[36:37] op_sel_hi:[0,1]
	s_waitcnt vmcnt(1)
	v_lshlrev_b32_e32 v40, 16, v138
	v_mfma_f32_16x16x32_bf16 v[32:35], v[226:229], v[210:213], v[100:103]
	v_mul_f32_e32 v36, v36, v40
	v_and_b32_e32 v40, 0xffff0000, v138
	v_pk_add_f32 v[38:39], v[134:135], v[38:39] op_sel_hi:[0,1]
	v_mul_f32_e32 v37, v37, v40
	v_lshlrev_b32_e32 v40, 16, v139
	v_mul_f32_e32 v36, 0x41000000, v36
	v_mul_f32_e32 v37, 0x41000000, v37
	v_mul_f32_e32 v38, v38, v40
	v_and_b32_e32 v40, 0xffff0000, v139
	v_mul_f32_e32 v39, v39, v40
	v_med3_f32 v36, v36, s51, v187
	v_med3_f32 v37, v37, s51, v187
	v_cvt_pk_fp8_f32 v246, v36, v37
	v_pk_add_f32 v[32:33], v[134:135], v[32:33] op_sel_hi:[0,1]
	s_waitcnt vmcnt(0)
	v_lshlrev_b32_e32 v36, 16, v136
	v_mul_f32_e32 v32, v32, v36
	v_and_b32_e32 v36, 0xffff0000, v136
	v_pk_add_f32 v[34:35], v[134:135], v[34:35] op_sel_hi:[0,1]
	v_mul_f32_e32 v33, v33, v36
	v_lshlrev_b32_e32 v36, 16, v137
	v_mul_f32_e32 v32, 0x41000000, v32
	v_mul_f32_e32 v33, 0x41000000, v33
	v_mul_f32_e32 v34, v34, v36
	v_and_b32_e32 v36, 0xffff0000, v137
	v_mul_f32_e32 v35, v35, v36
	v_med3_f32 v32, v32, s51, v187
	v_med3_f32 v33, v33, s51, v187
	v_cvt_pk_fp8_f32 v247, v32, v33
	v_mul_f32_e32 v88, 0x41000000, v88
	v_mul_f32_e32 v89, 0x41000000, v89
	v_or_b32_e32 v80, 16, v84
	v_mul_f32_e32 v74, 0x41000000, v74
	v_mul_f32_e32 v75, 0x41000000, v75
	v_mul_f32_e32 v70, 0x41000000, v70
	v_mul_f32_e32 v71, 0x41000000, v71
	v_or_b32_e32 v64, 32, v84
	v_mul_f32_e32 v58, 0x41000000, v58
	v_mul_f32_e32 v59, 0x41000000, v59
	v_mul_f32_e32 v54, 0x41000000, v54
	v_mul_f32_e32 v55, 0x41000000, v55
	v_or_b32_e32 v48, 48, v84
	v_mul_f32_e32 v42, 0x41000000, v42
	v_mul_f32_e32 v43, 0x41000000, v43
	v_mul_f32_e32 v38, 0x41000000, v38
	v_mul_f32_e32 v39, 0x41000000, v39
	v_mul_f32_e32 v34, 0x41000000, v34
	v_mul_f32_e32 v35, 0x41000000, v35
	v_med3_f32 v88, v88, s51, v187
	v_med3_f32 v89, v89, s51, v187
	v_ashrrev_i32_e32 v81, 31, v80
	v_med3_f32 v74, v74, s51, v187
	v_med3_f32 v75, v75, s51, v187
	v_med3_f32 v70, v70, s51, v187
	v_med3_f32 v71, v71, s51, v187
	v_ashrrev_i32_e32 v65, 31, v64
	v_med3_f32 v58, v58, s51, v187
	v_med3_f32 v59, v59, s51, v187
	v_med3_f32 v54, v54, s51, v187
	v_med3_f32 v55, v55, s51, v187
	v_ashrrev_i32_e32 v49, 31, v48
	v_med3_f32 v42, v42, s51, v187
	v_med3_f32 v43, v43, s51, v187
	v_med3_f32 v38, v38, s51, v187
	v_med3_f32 v39, v39, s51, v187
	v_med3_f32 v34, v34, s51, v187
	v_med3_f32 v35, v35, s51, v187
	v_cvt_pk_fp8_f32 v234, v88, v89 op_sel:[0,0,1]
	v_lshl_add_u64 v[80:81], s[20:21], 0, v[80:81]
	v_cvt_pk_fp8_f32 v237, v74, v75 op_sel:[0,0,1]
	v_cvt_pk_fp8_f32 v238, v70, v71 op_sel:[0,0,1]
	v_lshl_add_u64 v[64:65], s[20:21], 0, v[64:65]
	v_cvt_pk_fp8_f32 v241, v58, v59 op_sel:[0,0,1]
	v_cvt_pk_fp8_f32 v242, v54, v55 op_sel:[0,0,1]
	v_lshl_add_u64 v[48:49], s[20:21], 0, v[48:49]
	v_cvt_pk_fp8_f32 v245, v42, v43 op_sel:[0,0,1]
	v_cvt_pk_fp8_f32 v246, v38, v39 op_sel:[0,0,1]
	v_cvt_pk_fp8_f32 v247, v34, v35 op_sel:[0,0,1]
	v_lshlrev_b64 v[80:81], 11, v[80:81]
	v_lshlrev_b64 v[64:65], 11, v[64:65]
	v_lshlrev_b64 v[48:49], 11, v[48:49]
	v_lshl_add_u64 v[80:81], s[10:11], 0, v[80:81]
	v_lshl_add_u64 v[64:65], s[10:11], 0, v[64:65]
	v_lshl_add_u64 v[48:49], s[10:11], 0, v[48:49]
	s_addk_i32 s24, 0x100
	v_lshl_add_u64 v[76:77], v[80:81], 0, v[152:153]
	v_lshl_add_u64 v[60:61], v[64:65], 0, v[152:153]
	v_lshl_add_u64 v[44:45], v[48:49], 0, v[152:153]
	s_cmpk_eq_i32 s6, 0x1000
	v_permlane16_swap_b32_e32 v232, v233
	v_permlane16_swap_b32_e32 v234, v235
	v_permlane16_swap_b32_e32 v236, v237
	v_permlane16_swap_b32_e32 v238, v239
	v_permlane16_swap_b32_e32 v240, v241
	v_permlane16_swap_b32_e32 v242, v243
	v_permlane16_swap_b32_e32 v244, v245
	v_permlane16_swap_b32_e32 v246, v247
	v_lshl_add_u64 v[178:179], v[86:87], 0, v[248:249]
	v_lshl_add_u64 v[180:181], v[76:77], 0, v[248:249]
	v_lshl_add_u64 v[230:231], v[60:61], 0, v[248:249]
	v_lshl_add_u64 v[250:251], v[44:45], 0, v[248:249]
	v_permlane32_swap_b32_e32 v232, v234
	v_permlane32_swap_b32_e32 v233, v235
	v_permlane32_swap_b32_e32 v236, v238
	v_permlane32_swap_b32_e32 v237, v239
	v_permlane32_swap_b32_e32 v240, v242
	v_permlane32_swap_b32_e32 v241, v243
	v_permlane32_swap_b32_e32 v244, v246
	v_permlane32_swap_b32_e32 v245, v247
	s_nop 1
	global_store_dwordx4 v[178:179], v[232:235], off
	global_store_dwordx4 v[180:181], v[236:239], off
	global_store_dwordx4 v[230:231], v[240:243], off
	global_store_dwordx4 v[250:251], v[244:247], off
	s_barrier
	s_cbranch_scc1 .LBB0_279
